# norm3 slot reservation: per-expert serial LDS prefix loops over earlier waves replaced by one lane-parallel prefix (7 reads in flight) + readlane
# speedup vs baseline: 1.0130x; 1.0130x over previous
.LBB0_1331:
	s_or_b64 exec, exec, s[4:5]
	v_readlane_b32 s4, v242, 38
	s_waitcnt lgkmcnt(0)
	s_barrier
	v_readlane_b32 s101, v242, 36
	v_readfirstlane_b32 s100, v109
	v_and_b32_e32 v255, 15, v0
	v_lshlrev_b32_e32 v255, 2, v255
	v_add_u32_e32 v255, s101, v255
	ds_read_b32 v248, v255
	ds_read_b32 v249, v255 offset:64
	ds_read_b32 v250, v255 offset:128
	ds_read_b32 v251, v255 offset:192
	ds_read_b32 v252, v255 offset:256
	ds_read_b32 v253, v255 offset:320
	ds_read_b32 v254, v255 offset:384
	s_waitcnt lgkmcnt(0)
	s_cmp_gt_u32 s100, 0
	s_cselect_b32 s101, -1, 0
	v_and_b32_e32 v247, s101, v248
	s_cmp_gt_u32 s100, 1
	s_cselect_b32 s101, -1, 0
	v_and_b32_e32 v249, s101, v249
	v_add_u32_e32 v247, v247, v249
	s_cmp_gt_u32 s100, 2
	s_cselect_b32 s101, -1, 0
	v_and_b32_e32 v250, s101, v250
	v_add_u32_e32 v247, v247, v250
	s_cmp_gt_u32 s100, 3
	s_cselect_b32 s101, -1, 0
	v_and_b32_e32 v251, s101, v251
	v_add_u32_e32 v247, v247, v251
	s_cmp_gt_u32 s100, 4
	s_cselect_b32 s101, -1, 0
	v_and_b32_e32 v252, s101, v252
	v_add_u32_e32 v247, v247, v252
	s_cmp_gt_u32 s100, 5
	s_cselect_b32 s101, -1, 0
	v_and_b32_e32 v253, s101, v253
	v_add_u32_e32 v247, v247, v253
	s_cmp_gt_u32 s100, 6
	s_cselect_b32 s101, -1, 0
	v_and_b32_e32 v254, s101, v254
	v_add_u32_e32 v247, v247, v254
	v_mov_b32_e32 v18, s4
	ds_read_b32 v18, v18
	s_and_saveexec_b64 s[4:5], s[58:59]
	s_mov_b64 s[26:27], vcc
	s_cbranch_execz .LBB0_1341
	v_readlane_b32 s100, v247, 0
	s_waitcnt lgkmcnt(0)
	s_nop 0
	v_add_u32_e32 v18, s100, v18
.LBB0_1341:
	s_or_b64 exec, exec, s[4:5]
	v_readlane_b32 s4, v242, 46
	v_cndmask_b32_e64 v22, 0, 1, s[72:73]
	v_cmp_ne_u32_e64 s[68:69], 0, v22
	v_mov_b32_e32 v19, s4
	ds_read_b32 v19, v19
	v_cndmask_b32_e64 v22, 0, 1, s[66:67]
	v_cmp_ne_u32_e64 s[4:5], 0, v22
	s_nop 1
	v_writelane_b32 v241, s4, 59
	s_nop 1
	v_writelane_b32 v241, s5, 60
	s_and_saveexec_b64 s[4:5], s[58:59]
	s_cbranch_execz .LBB0_1351
	v_readlane_b32 s100, v247, 1
	s_waitcnt lgkmcnt(0)
	s_nop 0
	v_add_u32_e32 v19, s100, v19
.LBB0_1351:
	s_or_b64 exec, exec, s[4:5]
	v_readlane_b32 s4, v242, 48
	v_cndmask_b32_e64 v23, 0, 1, s[64:65]
	v_cmp_ne_u32_e64 s[76:77], 0, v23
	v_mov_b32_e32 v22, s4
	ds_read_b32 v22, v22
	v_cndmask_b32_e64 v23, 0, 1, s[0:1]
	v_cmp_ne_u32_e64 s[4:5], 0, v23
	s_nop 1
	v_writelane_b32 v241, s4, 61
	s_nop 1
	v_writelane_b32 v241, s5, 62
	s_and_saveexec_b64 s[4:5], s[58:59]
	s_cbranch_execz .LBB0_1361
	v_readlane_b32 s100, v247, 2
	s_waitcnt lgkmcnt(0)
	s_nop 0
	v_add_u32_e32 v22, s100, v22
.LBB0_1361:
	s_or_b64 exec, exec, s[4:5]
	v_readlane_b32 s4, v242, 50
	v_writelane_b32 v241, s62, 63
	s_nop 0
	v_mov_b32_e32 v23, s4
	ds_read_b32 v23, v23
	v_readlane_b32 s4, v241, 35
	v_cndmask_b32_e64 v24, 0, 1, s[62:63]
	v_readlane_b32 s5, v241, 36
	v_cmp_ne_u32_e64 s[80:81], 0, v24
	v_writelane_b32 v240, s63, 0
	v_cndmask_b32_e64 v24, 0, 1, s[4:5]
	v_cmp_ne_u32_e64 s[4:5], 0, v24
	s_nop 1
	v_writelane_b32 v240, s4, 1
	s_nop 1
	v_writelane_b32 v240, s5, 2
	s_and_saveexec_b64 s[4:5], s[58:59]
	s_cbranch_execz .LBB0_1371
	v_readlane_b32 s100, v247, 3
	s_waitcnt lgkmcnt(0)
	s_nop 0
	v_add_u32_e32 v23, s100, v23
.LBB0_1371:
	s_or_b64 exec, exec, s[4:5]
	v_readlane_b32 s4, v242, 52
	v_writelane_b32 v240, s60, 3
	s_nop 0
	v_mov_b32_e32 v24, s4
	ds_read_b32 v24, v24
	v_readlane_b32 s4, v241, 37
	v_cndmask_b32_e64 v25, 0, 1, s[60:61]
	v_readlane_b32 s5, v241, 38
	v_cmp_ne_u32_e64 s[84:85], 0, v25
	v_writelane_b32 v240, s61, 4
	v_cndmask_b32_e64 v25, 0, 1, s[4:5]
	v_cmp_ne_u32_e64 s[4:5], 0, v25
	s_nop 1
	v_writelane_b32 v240, s4, 5
	s_nop 1
	v_writelane_b32 v240, s5, 6
	s_and_saveexec_b64 s[4:5], s[58:59]
	s_cbranch_execz .LBB0_1381
	v_readlane_b32 s100, v247, 4
	s_waitcnt lgkmcnt(0)
	s_nop 0
	v_add_u32_e32 v24, s100, v24
.LBB0_1381:
	s_or_b64 exec, exec, s[4:5]
	v_readlane_b32 s4, v242, 54
	v_writelane_b32 v240, s52, 7
	s_nop 0
	v_mov_b32_e32 v25, s4
	ds_read_b32 v25, v25
	v_writelane_b32 v240, s53, 8
	v_cndmask_b32_e64 v26, 0, 1, s[52:53]
	v_cmp_ne_u32_e64 s[52:53], 0, v26
	v_writelane_b32 v240, s56, 9
	s_nop 1
	v_cndmask_b32_e64 v26, 0, 1, s[56:57]
	v_cmp_ne_u32_e64 s[86:87], 0, v26
	v_writelane_b32 v240, s57, 10
	s_and_saveexec_b64 s[4:5], s[58:59]
	s_cbranch_execz .LBB0_1391
	v_readlane_b32 s100, v247, 5
	s_waitcnt lgkmcnt(0)
	s_nop 0
	v_add_u32_e32 v25, s100, v25
.LBB0_1391:
	s_or_b64 exec, exec, s[4:5]
	v_readlane_b32 s4, v242, 56
	v_writelane_b32 v240, s54, 11
	s_nop 0
	v_mov_b32_e32 v26, s4
	ds_read_b32 v26, v26
	v_writelane_b32 v240, s55, 12
	v_cndmask_b32_e64 v27, 0, 1, s[54:55]
	v_cmp_ne_u32_e64 s[54:55], 0, v27
	v_writelane_b32 v240, s50, 13
	s_nop 1
	v_cndmask_b32_e64 v27, 0, 1, s[50:51]
	v_cmp_ne_u32_e64 s[88:89], 0, v27
	v_writelane_b32 v240, s51, 14
	s_and_saveexec_b64 s[4:5], s[58:59]
	s_cbranch_execz .LBB0_1401
	v_readlane_b32 s100, v247, 6
	s_waitcnt lgkmcnt(0)
	s_nop 0
	v_add_u32_e32 v26, s100, v26
.LBB0_1401:
	s_or_b64 exec, exec, s[4:5]
	v_readlane_b32 s4, v242, 58
	v_writelane_b32 v240, s48, 15
	s_nop 0
	v_mov_b32_e32 v27, s4
	ds_read_b32 v27, v27
	v_writelane_b32 v240, s49, 16
	v_cndmask_b32_e64 v28, 0, 1, s[48:49]
	v_cmp_ne_u32_e64 s[92:93], 0, v28
	v_writelane_b32 v240, s44, 17
	s_nop 1
	v_cndmask_b32_e64 v28, 0, 1, s[44:45]
	v_cmp_ne_u32_e64 s[56:57], 0, v28
	v_writelane_b32 v240, s45, 18
	s_and_saveexec_b64 s[4:5], s[58:59]
	s_cbranch_execz .LBB0_1411
	v_readlane_b32 s100, v247, 7
	s_waitcnt lgkmcnt(0)
	s_nop 0
	v_add_u32_e32 v27, s100, v27
.LBB0_1411:
	s_or_b64 exec, exec, s[4:5]
	v_readlane_b32 s4, v242, 60
	v_cndmask_b32_e64 v29, 0, 1, s[42:43]
	v_cmp_ne_u32_e64 s[70:71], 0, v29
	v_mov_b32_e32 v28, s4
	ds_read_b32 v28, v28
	v_cndmask_b32_e64 v29, 0, 1, s[38:39]
	s_mov_b64 s[62:63], s[42:43]
	s_mov_b64 s[60:61], s[38:39]
	v_cmp_ne_u32_e64 s[90:91], 0, v29
	s_and_saveexec_b64 s[4:5], s[58:59]
	s_cbranch_execz .LBB0_1421
	v_readlane_b32 s100, v247, 8
	s_waitcnt lgkmcnt(0)
	s_nop 0
	v_add_u32_e32 v28, s100, v28
.LBB0_1421:
	s_or_b64 exec, exec, s[4:5]
	v_readlane_b32 s4, v242, 62
	v_cndmask_b32_e64 v30, 0, 1, s[40:41]
	v_cmp_ne_u32_e64 s[78:79], 0, v30
	v_mov_b32_e32 v29, s4
	ds_read_b32 v29, v29
	v_cndmask_b32_e64 v30, 0, 1, s[36:37]
	s_mov_b64 s[38:39], s[40:41]
	s_mov_b64 s[44:45], s[36:37]
	v_cmp_ne_u32_e64 s[74:75], 0, v30
	s_and_saveexec_b64 s[4:5], s[58:59]
	s_cbranch_execz .LBB0_1431
	v_readlane_b32 s100, v247, 9
	s_waitcnt lgkmcnt(0)
	s_nop 0
	v_add_u32_e32 v29, s100, v29
.LBB0_1431:
	s_or_b64 exec, exec, s[4:5]
	v_readlane_b32 s4, v244, 0
	v_cndmask_b32_e64 v31, 0, 1, s[30:31]
	v_cmp_ne_u32_e64 s[94:95], 0, v31
	v_mov_b32_e32 v30, s4
	ds_read_b32 v30, v30
	v_readlane_b32 s4, v241, 39
	v_readlane_b32 s5, v241, 40
	s_mov_b64 s[42:43], s[30:31]
	s_nop 0
	v_cndmask_b32_e64 v31, 0, 1, s[4:5]
	v_cmp_ne_u32_e64 s[4:5], 0, v31
	s_and_saveexec_b64 s[6:7], s[58:59]
	s_cbranch_execz .LBB0_1441
	v_readlane_b32 s100, v247, 10
	s_waitcnt lgkmcnt(0)
	s_nop 0
	v_add_u32_e32 v30, s100, v30
.LBB0_1441:
	s_or_b64 exec, exec, s[6:7]
	v_readlane_b32 s6, v244, 2
	v_cndmask_b32_e64 v32, 0, 1, s[28:29]
	s_mov_b64 s[50:51], s[28:29]
	v_mov_b32_e32 v31, s6
	ds_read_b32 v31, v31
	v_cmp_ne_u32_e64 s[6:7], 0, v32
	v_cndmask_b32_e64 v32, 0, 1, s[24:25]
	s_mov_b64 s[48:49], s[24:25]
	v_cmp_ne_u32_e64 s[96:97], 0, v32
	s_and_saveexec_b64 s[8:9], s[58:59]
	s_cbranch_execz .LBB0_1451
	v_readlane_b32 s100, v247, 11
	s_waitcnt lgkmcnt(0)
	s_nop 0
	v_add_u32_e32 v31, s100, v31
.LBB0_1451:
	s_or_b64 exec, exec, s[8:9]
	v_readlane_b32 s8, v244, 4
	s_nop 1
	v_mov_b32_e32 v32, s8
	v_readlane_b32 s8, v241, 41
	ds_read_b32 v32, v32
	v_readlane_b32 s9, v241, 42
	s_nop 1
	v_cndmask_b32_e64 v33, 0, 1, s[8:9]
	v_readlane_b32 s8, v241, 43
	v_readlane_b32 s9, v241, 44
	v_cmp_ne_u32_e64 s[10:11], 0, v33
	s_nop 0
	v_cndmask_b32_e64 v33, 0, 1, s[8:9]
	v_cmp_ne_u32_e64 s[8:9], 0, v33
	s_and_saveexec_b64 s[12:13], s[58:59]
	s_cbranch_execz .LBB0_1461
	v_readlane_b32 s100, v247, 12
	s_waitcnt lgkmcnt(0)
	s_nop 0
	v_add_u32_e32 v32, s100, v32
.LBB0_1461:
	s_or_b64 exec, exec, s[12:13]
	v_readlane_b32 s12, v244, 6
	s_nop 1
	v_mov_b32_e32 v33, s12
	v_readlane_b32 s12, v241, 45
	ds_read_b32 v33, v33
	v_readlane_b32 s13, v241, 46
	s_nop 1
	v_cndmask_b32_e64 v34, 0, 1, s[12:13]
	v_readlane_b32 s12, v241, 47
	v_readlane_b32 s13, v241, 48
	v_cmp_ne_u32_e64 s[14:15], 0, v34
	s_nop 0
	v_cndmask_b32_e64 v34, 0, 1, s[12:13]
	v_cmp_ne_u32_e64 s[12:13], 0, v34
	s_and_saveexec_b64 s[16:17], s[58:59]
	s_cbranch_execz .LBB0_1471
	v_readlane_b32 s100, v247, 13
	s_waitcnt lgkmcnt(0)
	s_nop 0
	v_add_u32_e32 v33, s100, v33
.LBB0_1471:
	s_or_b64 exec, exec, s[16:17]
	v_readlane_b32 s16, v244, 8
	s_nop 1
	v_mov_b32_e32 v34, s16
	v_readlane_b32 s16, v241, 49
	ds_read_b32 v34, v34
	v_readlane_b32 s17, v241, 50
	s_nop 1
	v_cndmask_b32_e64 v35, 0, 1, s[16:17]
	v_readlane_b32 s16, v241, 51
	v_readlane_b32 s17, v241, 52
	v_cmp_ne_u32_e64 s[18:19], 0, v35
	s_nop 0
	v_cndmask_b32_e64 v35, 0, 1, s[16:17]
	v_cmp_ne_u32_e64 s[16:17], 0, v35
	s_and_saveexec_b64 s[20:21], s[58:59]
	s_cbranch_execz .LBB0_1481
	v_readlane_b32 s100, v247, 14
	s_waitcnt lgkmcnt(0)
	s_nop 0
	v_add_u32_e32 v34, s100, v34
.LBB0_1481:
	s_or_b64 exec, exec, s[20:21]
	v_readlane_b32 s20, v244, 10
	s_nop 1
	v_mov_b32_e32 v35, s20
	v_readlane_b32 s20, v241, 53
	ds_read_b32 v35, v35
	v_readlane_b32 s21, v241, 54
	s_nop 1
	v_cndmask_b32_e64 v36, 0, 1, s[20:21]
	v_readlane_b32 s20, v241, 55
	v_readlane_b32 s21, v241, 56
	v_cmp_ne_u32_e64 s[22:23], 0, v36
	s_nop 0
	v_cndmask_b32_e64 v36, 0, 1, s[20:21]
	v_cmp_ne_u32_e64 s[20:21], 0, v36
	s_and_saveexec_b64 s[24:25], s[58:59]
	s_cbranch_execz .LBB0_1491
	v_readlane_b32 s100, v247, 15
	s_waitcnt lgkmcnt(0)
	s_nop 0
	v_add_u32_e32 v35, s100, v35

	.amdhsa_kernel _Z4mega1Pii
		.amdhsa_group_segment_fixed_size 0
		.amdhsa_private_segment_fixed_size 0
		.amdhsa_kernarg_size 480
		.amdhsa_user_sgpr_count 2
		.amdhsa_user_sgpr_dispatch_ptr 0
		.amdhsa_user_sgpr_queue_ptr 0
		.amdhsa_user_sgpr_kernarg_segment_ptr 1
		.amdhsa_user_sgpr_dispatch_id 0
		.amdhsa_user_sgpr_kernarg_preload_length 0
		.amdhsa_user_sgpr_kernarg_preload_offset 0
		.amdhsa_user_sgpr_private_segment_size 0
		.amdhsa_uses_dynamic_stack 0
		.amdhsa_enable_private_segment 0
		.amdhsa_system_sgpr_workgroup_id_x 1
		.amdhsa_system_sgpr_workgroup_id_y 0
		.amdhsa_system_sgpr_workgroup_id_z 0
		.amdhsa_system_sgpr_workgroup_info 0
		.amdhsa_system_vgpr_workitem_id 0
		.amdhsa_next_free_vgpr 256
		.amdhsa_next_free_sgpr 102
		.amdhsa_accum_offset 256
		.amdhsa_reserve_vcc 1
		.amdhsa_float_round_mode_32 0
		.amdhsa_float_round_mode_16_64 0
		.amdhsa_float_denorm_mode_32 3
		.amdhsa_float_denorm_mode_16_64 3
		.amdhsa_dx10_clamp 1
		.amdhsa_ieee_mode 1
		.amdhsa_fp16_overflow 0
		.amdhsa_tg_split 0
		.amdhsa_exception_fp_ieee_invalid_op 0
		.amdhsa_exception_fp_denorm_src 0
		.amdhsa_exception_fp_ieee_div_zero 0
		.amdhsa_exception_fp_ieee_overflow 0
		.amdhsa_exception_fp_ieee_underflow 0
		.amdhsa_exception_fp_ieee_inexact 0
		.amdhsa_exception_int_div_zero 0
	.end_amdhsa_kernel

amdhsa.kernels:
  - .agpr_count:     0
    .args:
      - .offset:         0
        .size:           216
        .value_kind:     by_value
      - .offset:         216
        .size:           4
        .value_kind:     by_value
      - .offset:         220
        .size:           4
        .value_kind:     by_value
      - .offset:         224
        .size:           4
        .value_kind:     hidden_block_count_x
      - .offset:         228
        .size:           4
        .value_kind:     hidden_block_count_y
      - .offset:         232
        .size:           4
        .value_kind:     hidden_block_count_z
      - .offset:         236
        .size:           2
        .value_kind:     hidden_group_size_x
      - .offset:         238
        .size:           2
        .value_kind:     hidden_group_size_y
      - .offset:         240
        .size:           2
        .value_kind:     hidden_group_size_z
      - .offset:         242
        .size:           2
        .value_kind:     hidden_remainder_x
      - .offset:         244
        .size:           2
        .value_kind:     hidden_remainder_y
      - .offset:         246
        .size:           2
        .value_kind:     hidden_remainder_z
      - .offset:         264
        .size:           8
        .value_kind:     hidden_global_offset_x
      - .offset:         272
        .size:           8
        .value_kind:     hidden_global_offset_y
      - .offset:         280
        .size:           8
        .value_kind:     hidden_global_offset_z
      - .offset:         288
        .size:           2
        .value_kind:     hidden_grid_dims
      - .offset:         344
        .size:           4
        .value_kind:     hidden_dynamic_lds_size
    .group_segment_fixed_size: 0
    .kernarg_segment_align: 8
    .kernarg_segment_size: 480
    .language:       OpenCL C
    .language_version:
      - 2
      - 0
    .max_flat_workgroup_size: 512
    .name:           _Z4mega1Pii
    .private_segment_fixed_size: 0
    .sgpr_count:     108
    .sgpr_spill_count: 438
    .symbol:         _Z4mega1Pii.kd
    .uniform_work_group_size: 1
    .uses_dynamic_stack: false
    .vgpr_count:     256
    .vgpr_spill_count: 0
    .wavefront_size: 64
